# layer-1 MoE weight conversion moved from the neighbourhood-attention background task to the K/V-loader waves of the differential-attention loop (one 1 KB piece per 4-step iteration and wave)
# speedup vs baseline: 1.0104x; 1.0051x over previous
.LBB0_253:
	s_cmp_lt_i32 s30, 4
	s_cselect_b64 s[8:9], -1, 0
	s_and_b64 s[4:5], s[8:9], s[4:5]
	s_andn2_b64 vcc, exec, s[4:5]
	s_cbranch_vccnz .LBB0_364
	s_mov_b64 s[10:11], s[0:1]
	s_mov_b32 s98, 0x18000
	s_cmpk_eq_u32 s22, 0x100
	s_cselect_b32 s98, 0xc000, s98
	s_load_dwordx2 s[4:5], s[10:11], 0xd8
	v_readlane_b32 s12, v255, 6
	s_mul_i32 s6, s12, 0x2080
	v_mbcnt_hi_u32_b32 v4, -1, v208
	s_add_i32 s6, s6, 0
	s_waitcnt lgkmcnt(0)
	s_add_u32 s23, s4, 0x11800000
	v_lshlrev_b32_e32 v2, 2, v4
	v_and_b32_e32 v210, 60, v2
	v_lshlrev_b32_e32 v2, 3, v4
	s_addc_u32 s26, s5, 0
	v_and_b32_e32 v194, 24, v2
	v_ashrrev_i32_e32 v211, 2, v4
	s_add_u32 s27, s4, 0x1800000
	v_ashrrev_i32_e32 v209, 4, v4
	s_movk_i32 s7, 0x104
	v_mul_u32_u24_e32 v2, 0x104, v194
	v_mov_b32_e32 v3, 0
	v_and_b32_e32 v5, -4, v4
	v_add_u32_e32 v213, 16, v211
	v_add_u32_e32 v215, 32, v211
	v_add_u32_e32 v217, 48, v211
	s_addc_u32 s35, s5, 0
	s_mov_b32 s65, 0
	v_lshl_add_u32 v220, v210, 2, s6
	v_mul_lo_u32 v221, v209, s7
	v_mov_b32_e32 v195, v3
	v_add3_u32 v219, s6, v2, v5
	v_ashrrev_i32_e32 v212, 31, v211
	v_ashrrev_i32_e32 v214, 31, v213
	v_ashrrev_i32_e32 v216, 31, v215
	s_cmpk_gt_i32 s88, 0x81f
	v_ashrrev_i32_e32 v218, 31, v217
	s_cbranch_scc1 .LBB0_352
	s_add_u32 s15, s4, 0x25b00000
	s_addc_u32 s48, s5, 0
	s_add_u32 s49, s4, 0x29c00000
	s_addc_u32 s50, s5, 0
	s_add_u32 s51, s4, 0x2dd00000
	s_addc_u32 s53, s5, 0
	v_and_b32_e32 v2, 31, v4
	v_ashrrev_i32_e32 v4, 3, v4
	s_lshl_b32 s54, s12, 5
	s_lshr_b32 s55, s3, 7
	v_and_b32_e32 v222, -4, v4
	v_lshl_add_u64 v[4:5], s[4:5], 0, v[2:3]
	s_mov_b64 s[4:5], 0x31e00000
	v_and_or_b32 v2, s54, 32, v2
	s_cmp_lg_u32 0, -1
	v_lshl_add_u64 v[196:197], v[4:5], 0, s[4:5]
	v_sub_u32_e64 v4, v2, 8 clamp
	s_cselect_b32 s4, 0, 0
	s_and_b32 s3, s3, 0xffffff80
	v_min_u32_e32 v223, 48, v4
	s_sub_i32 s3, s4, s3
	v_sub_u32_e32 v224, 15, v2
	v_add_u32_e32 v225, 16, v223
	s_mov_b32 s13, 0
	s_add_i32 s3, s3, 0x8800
	s_mov_b64 s[20:21], 0
	s_mov_b64 s[18:19], 0
	s_mov_b32 s56, 0x41000000
	s_mov_b32 s14, 0x42000000
	s_movk_i32 s57, 0x1e0
	s_movk_i32 s58, 0xffdf
	s_add_i32 s59, 0, 0x4000
	s_mov_b32 s60, s88
	s_mov_b32 s61, s88
	s_mov_b32 s63, 0
	s_mov_b32 s62, s52
	s_cmpk_gt_i32 s61, 0x7ff
	s_mov_b64 s[4:5], -1
	s_cbranch_scc0 .LBB0_290
	s_branch .LBB0_257

.LBB0_276:
	s_cmp_lt_i32 s64, s98
	s_cselect_b64 s[6:7], -1, 0
	s_cmp_ge_i32 s64, s98
	s_cbranch_scc1 .LBB0_282
	s_ashr_i32 s65, s64, 1
	s_mul_hi_i32 s12, s65, 0x2aaaaaab
	s_lshr_b32 s28, s12, 31
	s_ashr_i32 s67, s12, 12
	s_add_i32 s67, s67, s28
	s_mul_i32 s68, s67, 0xffffa000
	s_lshl_b32 s12, s64, 5
	s_add_i32 s68, s68, s65
	s_and_b32 s66, s12, 32
	s_cmpk_gt_i32 s68, 0x3fff
	s_mov_b64 s[46:47], -1
	s_cbranch_scc0 .LBB0_279
	s_add_i32 s12, s68, 0xffffc000
	s_load_dwordx2 s[42:43], s[10:11], 0xc0
	s_lshl_b32 s28, s67, 5
	s_lshr_b32 s12, s12, 8
	s_add_i32 s28, s12, s28
	s_lshl_b32 s12, s65, 2
	s_and_b32 s12, s12, 0x3c0
	s_ashr_i32 s29, s28, 31
	s_or_b32 s12, s12, s66
	s_lshl_b64 s[44:45], s[28:29], 20
	s_lshl_b64 s[28:29], s[28:29], 22
	s_waitcnt lgkmcnt(0)
	s_add_u32 s28, s42, s28
	s_addc_u32 s29, s43, s29
	s_lshl_b32 s42, s12, 12
	s_add_u32 s42, s28, s42
	s_addc_u32 s43, s29, 0
	s_lshl_b32 s28, s65, 6
	s_and_b32 s28, s28, 0x3c0
	s_lshl_b32 s46, s28, 2
	s_add_u32 s42, s42, s46
	s_addc_u32 s43, s43, 0
	s_add_u32 s44, s23, s44
	s_mov_b32 s29, s13
	s_addc_u32 s45, s26, s45
	s_mov_b64 s[46:47], 0

.LBB0_323:
	s_cmp_lt_i32 s62, s98
	s_cselect_b64 s[20:21], -1, 0
	s_cmp_ge_i32 s62, s98
	s_cbranch_scc1 .LBB0_329
	s_ashr_i32 s63, s62, 1
	s_mul_hi_i32 s12, s63, 0x2aaaaaab
	s_lshr_b32 s18, s12, 31
	s_ashr_i32 s75, s12, 12
	s_add_i32 s75, s75, s18
	s_mul_i32 s76, s75, 0xffffa000
	s_lshl_b32 s12, s62, 5
	s_add_i32 s76, s76, s63
	s_and_b32 s74, s12, 32
	s_cmpk_gt_i32 s76, 0x3fff
	s_mov_b64 s[42:43], -1
	s_cbranch_scc0 .LBB0_326
	s_add_i32 s12, s76, 0xffffc000
	s_load_dwordx2 s[38:39], s[10:11], 0xc0
	s_lshl_b32 s18, s75, 5
	s_lshr_b32 s12, s12, 8
	s_add_i32 s18, s12, s18
	s_lshl_b32 s12, s63, 2
	s_and_b32 s12, s12, 0x3c0
	s_ashr_i32 s19, s18, 31
	s_or_b32 s12, s12, s74
	s_lshl_b64 s[40:41], s[18:19], 20
	s_lshl_b64 s[18:19], s[18:19], 22
	s_waitcnt lgkmcnt(0)
	s_add_u32 s18, s38, s18
	s_addc_u32 s19, s39, s19
	s_lshl_b32 s38, s12, 12
	s_add_u32 s38, s18, s38
	s_addc_u32 s39, s19, 0
	s_lshl_b32 s18, s63, 6
	s_and_b32 s18, s18, 0x3c0
	s_lshl_b32 s42, s18, 2
	s_add_u32 s38, s38, s42
	s_addc_u32 s39, s39, 0
	s_add_u32 s40, s23, s40
	s_mov_b32 s19, s13
	s_addc_u32 s41, s26, s41
	s_mov_b64 s[42:43], 0

.LBB0_353:
	s_cmp_lt_i32 s64, s98
	s_cselect_b64 s[14:15], -1, 0
	s_or_b64 s[4:5], s[6:7], s[14:15]
	s_andn2_b64 vcc, exec, s[4:5]
	s_cbranch_vccnz .LBB0_364
	v_add_u32_e32 v2, v220, v221
	s_mov_b32 s4, 0x42000000
	v_add_u32_e32 v4, 0x9000, v2
	v_add_u32_e32 v5, 0x9008, v2
	v_add_u32_e32 v6, 0x9410, v2
	v_add_u32_e32 v7, 0x9418, v2
	v_add_u32_e32 v8, 0x9820, v2
	v_add_u32_e32 v9, 0x9828, v2
	v_add_u32_e32 v10, 0x9c30, v2
	v_add_u32_e32 v11, 0x9c38, v2
	v_add_u32_e32 v12, 0xa040, v2
	v_add_u32_e32 v13, 0xa048, v2
	v_add_u32_e32 v14, 0xa450, v2
	v_add_u32_e32 v15, 0xa458, v2
	v_add_u32_e32 v16, 0xa860, v2
	v_add_u32_e32 v17, 0xa868, v2
	v_add_u32_e32 v18, 0xac70, v2
	v_add_u32_e32 v19, 0xac78, v2
	v_mov_b32_e32 v3, 0
	s_mov_b32 s13, 0
	v_add_u32_e32 v20, 0x9000, v219
	v_add_u32_e32 v21, 0x9400, v219
	s_branch .LBB0_357

.LBB0_356:
	s_cmp_lt_i32 s64, s98
	s_cselect_b64 s[14:15], -1, 0
	s_or_b64 s[16:17], s[6:7], s[14:15]
	s_and_b64 vcc, exec, s[16:17]
	s_cbranch_vccz .LBB0_364

.LBB0_1198:
	s_cmp_ge_i32 s53, s35
	s_cbranch_scc1 .LBB0_1428
	s_load_dwordx2 s[14:15], s[10:11], 0xd8
	v_mov_b32_e32 v1, 0x3fb8aa3b
	v_mul_f32_e32 v3, s7, v1
	v_mul_f32_e32 v1, s3, v1
	v_mul_f32_e32 v2, 0x4f7ffffe, v2
	s_waitcnt lgkmcnt(0)
	s_add_u32 s3, s14, 0x25b00000
	s_addc_u32 s8, s15, 0
	s_add_u32 s16, s14, 0x29c00000
	s_addc_u32 s17, s15, 0
	s_add_u32 s9, s14, 0x3a000000
	s_addc_u32 s26, s15, 0
	v_cvt_u32_f32_e32 v2, v2
	s_add_u32 s27, s14, 0x31e00000
	s_addc_u32 s23, s15, 0
	v_writelane_b32 v255, s20, 8
	s_and_b64 s[18:19], s[12:13], exec
	s_cselect_b32 s18, s6, s22
	v_writelane_b32 v255, s21, 9
	s_sub_i32 s21, 0, s6
	v_readfirstlane_b32 s28, v2
	s_mul_i32 s21, s21, s28
	s_mul_hi_u32 s21, s28, s21
	s_abs_i32 s20, s88
	s_add_i32 s28, s28, s21
	s_mul_hi_u32 s21, s20, s28
	s_mul_i32 s28, s21, s6
	v_readlane_b32 s7, v255, 6
	s_sub_i32 s20, s20, s28
	s_lshl_b32 s19, s7, 5
	s_ashr_i32 s7, s88, 31
	s_add_i32 s28, s21, 1
	s_sub_i32 s29, s20, s6
	s_cmp_ge_u32 s20, s6
	v_exp_f32_e32 v3, v3
	v_exp_f32_e32 v1, v1
	s_cselect_b32 s21, s28, s21
	s_cselect_b32 s20, s29, s20
	s_add_i32 s28, s21, 1
	s_cmp_ge_u32 s20, s6
	s_cselect_b32 s6, s28, s21
	v_sub_f32_e32 v1, v3, v1
	v_lshl_add_u32 v3, v0, 2, 0
	s_xor_b32 s6, s6, s7
	v_cndmask_b32_e64 v2, 0, 1, s[4:5]
	v_add_f32_e32 v1, 0x3eb60549, v1
	s_mov_b32 s36, 0
	v_add_u32_e32 v179, 0xc800, v3
	s_sub_i32 s20, s6, s7
	v_cmp_ne_u32_e64 s[4:5], 1, v2
	s_movk_i32 s21, 0xffc0
	v_mov_b32_e32 v181, 0
	s_mov_b32 s54, 0x41000000
	s_mov_b64 s[56:57], 0x3a004000
	s_mov_b64 s[58:59], 0x3a005000
	s_mov_b64 s[60:61], 0x3a006000
	s_mov_b64 s[62:63], 0x3a007000
	s_mov_b64 s[64:65], 0x3a008000
	s_mov_b64 s[66:67], 0x3a009000
	s_mov_b64 s[68:69], 0x3a00a000
	s_mov_b64 s[70:71], 0x3a00b000
	s_mov_b64 s[72:73], 0x8000
	s_mov_b64 s[74:75], 0x40000
	s_mov_b64 s[82:83], 0x206000
	s_mov_b64 s[84:85], 0x207000
	s_load_dwordx2 s[100:101], s[0:1], 0xb0
	s_waitcnt lgkmcnt(0)
	s_add_u32 s100, s100, 0x10000000
	s_addc_u32 s101, s101, 0
	v_writelane_b32 v254, s100, 0
	v_writelane_b32 v254, s101, 1
	s_load_dwordx2 s[100:101], s[0:1], 0xc0
	s_waitcnt lgkmcnt(0)
	s_add_u32 s100, s100, 0x8000000
	s_addc_u32 s101, s101, 0
	v_writelane_b32 v254, s100, 2
	v_writelane_b32 v254, s101, 3
	s_load_dwordx2 s[100:101], s[0:1], 0xd8
	s_waitcnt lgkmcnt(0)
	v_writelane_b32 v254, s100, 4
	v_writelane_b32 v254, s101, 5
	v_readfirstlane_b32 s100, v0
	s_lshr_b32 s100, s100, 6
	s_lshl_b32 s101, s2, 2
	s_add_i32 s100, s100, s101
	s_lshr_b32 s101, s100, 5
	s_lshl_b32 s101, s101, 15
	s_and_b32 s98, s100, 31
	s_lshl_b32 s98, s98, 8
	s_add_i32 s101, s101, s98
	v_writelane_b32 v254, s101, 6
	s_and_b32 s98, s100, 15
	s_lshr_b32 s98, s98, 1
	s_lshl_b32 s98, s98, 8
	s_bfe_u32 s99, s100, 0x10004
	s_lshl_b32 s99, s99, 7
	s_add_i32 s98, s98, s99
	s_and_b32 s99, s100, 1
	s_lshl_b32 s99, s99, 6
	s_add_i32 s98, s98, s99
	s_lshl_b32 s98, s98, 10
	s_lshr_b32 s99, s100, 5
	s_lshl_b32 s99, s99, 2
	s_add_i32 s98, s98, s99
	s_add_i32 s98, s98, 0x5800000
	v_writelane_b32 v254, s98, 7
	s_lshr_b32 s98, s100, 4
	s_lshl_b32 s99, s98, 14
	s_and_b32 s101, s100, 15
	s_lshl_b32 s101, s101, 8
	s_add_i32 s99, s99, s101
	v_writelane_b32 v254, s99, 8
	s_lshl_b32 s99, s98, 2
	s_and_b32 s101, s100, 15
	s_lshl_b32 s101, s101, 16
	s_add_i32 s99, s99, s101
	s_add_i32 s99, s99, 0x13800000
	v_writelane_b32 v254, s99, 9
	v_and_b32_e32 v240, 63, v0
	v_lshrrev_b32_e32 v252, 4, v240
	v_and_b32_e32 v253, 15, v240
	v_lshlrev_b32_e32 v243, 4, v253
	v_lshl_add_u32 v240, v252, 13, v243
	v_lshl_add_u32 v242, v252, 12, v243
	v_lshl_add_u32 v253, v253, 2, v252
	v_lshlrev_b32_e32 v253, 10, v253
	v_mov_b32_e32 v252, v242
	s_cmpk_eq_u32 s22, 0x100
	s_cselect_b32 s32, 0, 0x180
	s_mov_b32 s98, 0
	s_mov_b32 s99, 0
	v_mov_b32_e32 v184, 0x3727c5ac
	s_mov_b32 s55, 0xf800000
	v_mov_b32_e32 v185, 0x260
	s_branch .LBB0_1203

.LBB0_1264:
	s_lshl_b32 s94, s77, 8
	s_add_i32 s77, s94, 0x8000
	s_and_b64 vcc, exec, s[38:39]
	s_cbranch_vccz .LBB0_1317
	ds_read_b128 v[18:21], v183 offset:0
	ds_read_b128 v[22:25], v190 offset:0
	ds_read_b128 v[34:37], v183 offset:0x800
	ds_read_b128 v[38:41], v190 offset:0x800
	s_waitcnt lgkmcnt(0)
	s_waitcnt vmcnt(0)
	s_nop 9
	v_mfma_f32_32x32x64_f8f6f4 v[18:33], v[18:25], v[154:161], 0
	s_mov_b32 s37, s36
	s_mov_b32 s38, s36
	s_mov_b32 s39, s36
	s_mov_b32 s40, s36
	s_mov_b32 s41, s36
	s_mov_b32 s42, s36
	s_mov_b32 s43, s36
	s_mov_b32 s44, s36
	s_mov_b32 s45, s36
	s_mov_b32 s46, s36
	s_mov_b32 s47, s36
	s_mov_b32 s48, s36
	s_mov_b32 s49, s36
	s_mov_b32 s50, s36
	s_mov_b32 s51, s36
	v_mov_b64_e32 v[2:3], s[36:37]
	v_mov_b64_e32 v[4:5], s[38:39]
	v_mov_b64_e32 v[6:7], s[40:41]
	v_mov_b64_e32 v[8:9], s[42:43]
	v_mov_b64_e32 v[10:11], s[44:45]
	v_mov_b64_e32 v[12:13], s[46:47]
	v_mov_b64_e32 v[14:15], s[48:49]
	v_mov_b64_e32 v[16:17], s[50:51]
	v_max_f32_e32 v42, v19, v19
	v_max_f32_e32 v43, v18, v18
	v_max_f32_e32 v42, v43, v42
	v_max3_f32 v42, v42, v20, v21
	v_max3_f32 v42, v42, v22, v23
	v_max3_f32 v42, v42, v24, v25
	v_max3_f32 v42, v42, v26, v27
	v_max3_f32 v42, v42, v28, v29
	v_max3_f32 v50, v42, v30, v31
	v_mfma_f32_32x32x64_f8f6f4 v[34:49], v[34:41], v[154:161], 0
	v_max3_f32 v50, v50, v32, v33
	s_lshl_b32 s45, s81, 10
	s_lshl_b32 s46, s80, 10
	s_cmp_lg_u32 0, -1
	s_cselect_b32 s38, 0, 0
	s_add_i32 s37, s38, 0x2000
	s_add_i32 s39, s38, 0x3000
	s_add_i32 s6, s38, 0x1000
	v_add_u32_e32 v203, s37, v194
	s_add_i32 s37, s38, 0x6000
	v_add_u32_e32 v199, s39, v194
	s_add_i32 s39, s38, 0x8000
	s_add_i32 s38, s38, 0xa000
	v_add_u32_e32 v205, s6, v194
	v_add_u32_e32 v201, s37, v194
	s_nop 4
	v_max3_f32 v50, v50, v34, v35
	v_max3_f32 v50, v50, v36, v37
	v_max3_f32 v50, v50, v38, v39
	v_max3_f32 v50, v50, v40, v41
	v_max3_f32 v50, v50, v42, v43
	v_max3_f32 v50, v50, v44, v45
	v_max3_f32 v50, v50, v46, v47
	v_max3_f32 v50, v50, v48, v49
	v_mov_b32_e32 v51, v50
	s_nop 1
	v_permlane32_swap_b32_e32 v50, v51
	v_max_f32_e32 v51, v51, v51
	v_max_f32_e32 v50, v50, v50
	v_max_f32_e32 v50, v50, v51
	s_cmp_eq_u32 s98, 0
	s_cselect_b32 s100, 0x40000000, 0xc0600000
	v_add_f32_e32 v198, s100, v50
	v_add_u32_e32 v196, s39, v194
	v_add_u32_e32 v194, s38, v194
	s_lshl_b32 s38, s95, 4
	v_sub_f32_e32 v18, v18, v198
	s_and_b32 s38, s38, 0xfffffc00
	s_ashr_i32 s89, s88, 31
	v_exp_f32_e32 v114, v18
	s_or_b32 s40, s88, 0x100
	s_add_i32 s41, s94, 0x4100
	s_or_b32 s42, s88, 0x140
	s_add_i32 s43, s94, 0x4140
	v_lshl_or_b32 v18, v193, 4, s38
	s_lshl_b64 s[38:39], s[88:89], 10
	s_add_u32 s38, s38, s87
	v_xor_b32_e32 v82, 0x80000000, v198
	v_sub_f32_e32 v34, v34, v198
	v_sub_f32_e32 v19, v19, v198
	v_sub_f32_e32 v35, v35, v198
	v_sub_f32_e32 v20, v20, v198
	v_sub_f32_e32 v36, v36, v198
	v_sub_f32_e32 v21, v21, v198
	v_sub_f32_e32 v37, v37, v198
	v_sub_f32_e32 v22, v22, v198
	v_sub_f32_e32 v38, v38, v198
	v_sub_f32_e32 v23, v23, v198
	v_sub_f32_e32 v39, v39, v198
	v_sub_f32_e32 v24, v24, v198
	v_sub_f32_e32 v40, v40, v198
	v_sub_f32_e32 v25, v25, v198
	v_sub_f32_e32 v41, v41, v198
	v_sub_f32_e32 v26, v26, v198
	v_sub_f32_e32 v42, v42, v198
	v_sub_f32_e32 v27, v27, v198
	v_sub_f32_e32 v43, v43, v198
	v_sub_f32_e32 v28, v28, v198
	v_sub_f32_e32 v44, v44, v198
	v_sub_f32_e32 v29, v29, v198
	v_sub_f32_e32 v45, v45, v198
	v_sub_f32_e32 v30, v30, v198
	v_sub_f32_e32 v46, v46, v198
	v_sub_f32_e32 v31, v31, v198
	v_sub_f32_e32 v47, v47, v198
	v_sub_f32_e32 v32, v32, v198
	v_sub_f32_e32 v48, v48, v198
	v_sub_f32_e32 v33, v33, v198
	v_sub_f32_e32 v49, v49, v198
	s_addc_u32 s39, s39, s76
	v_mov_b32_e32 v83, v82
	v_mov_b32_e32 v84, v82
	v_mov_b32_e32 v85, v82
	v_mov_b32_e32 v86, v82
	v_mov_b32_e32 v87, v82
	v_mov_b32_e32 v88, v82
	v_mov_b32_e32 v89, v82
	v_mov_b32_e32 v90, v82
	v_mov_b32_e32 v91, v82
	v_mov_b32_e32 v92, v82
	v_mov_b32_e32 v93, v82
	v_mov_b32_e32 v94, v82
	v_mov_b32_e32 v95, v82
	v_mov_b32_e32 v96, v82
	v_mov_b32_e32 v97, v82
	v_exp_f32_e32 v98, v34
	v_exp_f32_e32 v115, v19
	v_exp_f32_e32 v99, v35
	v_exp_f32_e32 v116, v20
	v_exp_f32_e32 v100, v36
	v_exp_f32_e32 v117, v21
	v_exp_f32_e32 v101, v37
	v_exp_f32_e32 v118, v22
	v_exp_f32_e32 v102, v38
	v_exp_f32_e32 v119, v23
	v_exp_f32_e32 v103, v39
	v_exp_f32_e32 v120, v24
	v_exp_f32_e32 v104, v40
	v_exp_f32_e32 v121, v25
	v_exp_f32_e32 v105, v41
	v_exp_f32_e32 v122, v26
	v_exp_f32_e32 v106, v42
	v_exp_f32_e32 v123, v27
	v_exp_f32_e32 v107, v43
	v_exp_f32_e32 v124, v28
	v_exp_f32_e32 v108, v44
	v_exp_f32_e32 v125, v29
	v_exp_f32_e32 v109, v45
	v_exp_f32_e32 v126, v30
	v_exp_f32_e32 v110, v46
	v_exp_f32_e32 v127, v31
	v_exp_f32_e32 v111, v47
	v_exp_f32_e32 v128, v32
	v_exp_f32_e32 v112, v48
	v_exp_f32_e32 v129, v33
	v_exp_f32_e32 v113, v49
	v_mov_b32_e32 v19, v181
	s_add_u32 s38, s38, 0x29c30000
	s_waitcnt vmcnt(3) lgkmcnt(0)
	s_barrier
	v_lshl_add_u64 v[172:173], s[92:93], 0, v[18:19]
	s_addc_u32 s39, s39, 0
	v_add3_u32 v18, s79, v191, v192
	v_lshl_add_u64 v[174:175], s[38:39], 0, v[18:19]
	v_mov_b32_e32 v162, 0
	v_mov_b64_e32 v[48:49], v[16:17]
	v_mov_b64_e32 v[64:65], v[16:17]
	v_mov_b64_e32 v[80:81], v[16:17]
	v_mov_b64_e32 v[32:33], v[16:17]
	v_lshl_add_u64 v[170:171], s[28:29], 0, v[180:181]
	v_add_u32_e32 v206, v205, v195
	v_cmp_gt_u32_e64 s[6:7], 32, v193
	v_add_u32_e32 v204, v203, v195
	v_add_u32_e32 v202, v201, v195
	s_movk_i32 s37, 0x100
	v_add_u32_e32 v200, v199, v195
	v_add_u32_e32 v197, v196, v195
	v_add_u32_e32 v195, v194, v195
	s_mov_b32 s44, -3
	s_add_i32 s45, s45, 0
	s_add_i32 s46, s46, 0
	v_mov_b64_e32 v[46:47], v[14:15]
	v_mov_b64_e32 v[44:45], v[12:13]
	v_mov_b64_e32 v[42:43], v[10:11]
	v_mov_b64_e32 v[40:41], v[8:9]
	v_mov_b64_e32 v[38:39], v[6:7]
	v_mov_b64_e32 v[36:37], v[4:5]
	v_mov_b64_e32 v[34:35], v[2:3]
	v_mov_b64_e32 v[62:63], v[14:15]
	v_mov_b64_e32 v[60:61], v[12:13]
	v_mov_b64_e32 v[58:59], v[10:11]
	v_mov_b64_e32 v[56:57], v[8:9]
	v_mov_b64_e32 v[54:55], v[6:7]
	v_mov_b64_e32 v[52:53], v[4:5]
	v_mov_b64_e32 v[50:51], v[2:3]
	v_mov_b64_e32 v[78:79], v[14:15]
	v_mov_b64_e32 v[76:77], v[12:13]
	v_mov_b64_e32 v[74:75], v[10:11]
	v_mov_b64_e32 v[72:73], v[8:9]
	v_mov_b64_e32 v[70:71], v[6:7]
	v_mov_b64_e32 v[68:69], v[4:5]
	v_mov_b64_e32 v[66:67], v[2:3]
	v_mov_b64_e32 v[30:31], v[14:15]
	v_mov_b64_e32 v[28:29], v[12:13]
	v_mov_b64_e32 v[26:27], v[10:11]
	v_mov_b64_e32 v[24:25], v[8:9]
	v_mov_b64_e32 v[22:23], v[6:7]
	v_mov_b64_e32 v[20:21], v[4:5]
	v_mov_b64_e32 v[18:19], v[2:3]
	v_mov_b32_e32 v163, v162
	v_mov_b32_e32 v164, v162
	v_mov_b32_e32 v165, v162
	v_mov_b32_e32 v166, v162
	v_mov_b32_e32 v167, v162
	v_mov_b32_e32 v168, v162
	v_mov_b32_e32 v169, v162
	s_and_b32 s32, s32, 0x5fffffff
	s_cmp_lg_u32 s98, 0
	s_cbranch_scc1 .LBB0_1268
	s_branch .Lf_1268

.LBB0_1267:
	s_bitcmp1_b32 s32, 31
	s_cbranch_scc1 .Lkc_w3r_r0
	s_waitcnt vmcnt(3) lgkmcnt(0)
	s_branch .Lkc_w3e_r0
.Lkc_w3r_r0:
	s_waitcnt vmcnt(4) lgkmcnt(0)
	s_bitset0_b32 s32, 31
.Lkc_w3e_r0:
	s_barrier
	s_addk_i32 s37, 0x100
	v_lshl_add_u64 v[172:173], v[172:173], 0, s[72:73]
	s_cmpk_lt_u32 s44, 0xfa
	v_lshl_add_u64 v[174:175], v[174:175], 0, s[74:75]
	s_cbranch_scc0 .LBB0_1295
.LBB0_1268:
	s_add_i32 s49, s45, 0x3000
	v_lshl_add_u64 v[130:131], s[14:15], 0, v[174:175]
	s_mov_b32 m0, s49
	v_lshl_add_u64 v[176:177], s[14:15], 0, v[172:173]
	s_add_i32 s47, s46, 0x8000
	global_load_lds_dwordx4 v[130:131], off
	v_lshl_add_u64 v[130:131], v[176:177], 0, s[56:57]
	s_mov_b32 m0, s47
	s_add_i32 s48, s46, 0x9000
	global_load_lds_dwordx4 v[130:131], off
	v_lshl_add_u64 v[130:131], v[176:177], 0, s[58:59]
	s_mov_b32 m0, s48
	v_cvt_pk_fp8_f32 v162, v114, v115
	global_load_lds_dwordx4 v[130:131], off
	s_and_b32 s100, s32, 0x3ff
	s_cmpk_lt_u32 s100, 0x180
	s_cbranch_scc0 .Lkc_i9_r0
	s_cmpk_lt_u32 s100, 0x100
	s_cbranch_scc0 .Lkc_id_r0
	s_lshr_b32 s101, s100, 3
	s_lshl_b32 s101, s101, 23
	s_and_b32 s100, s100, 7
	s_lshl_b32 s100, s100, 20
	s_add_i32 s100, s100, s101
	v_readlane_b32 s101, v254, 6
	s_add_i32 s100, s100, s101
	v_add_u32_e32 v238, s100, v240
	v_readlane_b32 s100, v254, 0
	v_readlane_b32 s101, v254, 1
	s_branch .Lkc_ij_r0
.Lkc_id_r0:
	s_sub_i32 s100, s100, 0x100
	s_lshr_b32 s101, s100, 2
	s_lshl_b32 s101, s101, 22
	s_and_b32 s100, s100, 3
	s_lshl_b32 s100, s100, 20
	s_add_i32 s100, s100, s101
	v_readlane_b32 s101, v254, 8
	s_add_i32 s100, s100, s101
	v_add_u32_e32 v238, s100, v252
	v_readlane_b32 s100, v254, 2
	v_readlane_b32 s101, v254, 3
.Lkc_ij_r0:
	v_mov_b32_e32 v239, 0
	s_nop 1
	v_lshl_add_u64 v[238:239], v[238:239], 0, s[100:101]
	global_load_dwordx4 v[234:237], v[238:239], off
	s_or_b32 s32, s32, 0xc0000000
.Lkc_i9_r0:
	v_cvt_pk_fp8_f32 v163, v118, v119
	ds_read_b128 v[130:133], v205 offset:0
	ds_read_b128 v[134:137], v206 offset:0
	ds_read_b128 v[210:213], v205 offset:0x800
	ds_read_b128 v[214:217], v206 offset:0x800
	v_cvt_pk_fp8_f32 v162, v116, v117 op_sel:[0,0,1]
	v_cvt_pk_fp8_f32 v163, v120, v121 op_sel:[0,0,1]
	s_waitcnt lgkmcnt(2)
	v_cvt_pk_fp8_f32 v164, v122, v123
	v_cvt_pk_fp8_f32 v165, v126, v127
	ds_read_b128 v[218:221], v188 offset:0
	ds_read_b128 v[222:225], v189 offset:0
	v_cvt_pk_fp8_f32 v164, v124, v125 op_sel:[0,0,1]
	v_cvt_pk_fp8_f32 v165, v128, v129 op_sel:[0,0,1]
	v_mfma_f32_32x32x64_f8f6f4 v[114:129], v[130:137], v[154:161], v[82:97]
	s_waitcnt lgkmcnt(2)
	v_mfma_f32_32x32x64_f8f6f4 v[130:145], v[210:217], v[154:161], v[82:97]
	v_cvt_pk_fp8_f32 v166, v98, v99
	v_cvt_pk_fp8_f32 v167, v102, v103
	v_cvt_pk_fp8_f32 v168, v106, v107
	v_cvt_pk_fp8_f32 v169, v110, v111
	v_cvt_pk_fp8_f32 v166, v100, v101 op_sel:[0,0,1]
	v_cvt_pk_fp8_f32 v167, v104, v105 op_sel:[0,0,1]
	v_cvt_pk_fp8_f32 v168, v108, v109 op_sel:[0,0,1]
	v_cvt_pk_fp8_f32 v169, v112, v113 op_sel:[0,0,1]
	s_nop 0
	ds_read_b128 v[106:109], v188 offset:0x800
	ds_read_b128 v[110:113], v189 offset:0x800
	s_nop 0
	v_mfma_f32_16x16x128_f8f6f4 v[18:21], v[162:169], v[146:153], v[18:21]
	s_waitcnt lgkmcnt(2)
	v_mfma_f32_32x32x64_f8f6f4 v[2:17], v[162:169], v[218:225], v[2:17]
	ds_read_b128 v[98:101], v188 offset:0x1000
	ds_read_b128 v[102:105], v189 offset:0x1000
	v_max3_f32 v191, v114, v115, v116
	v_max3_f32 v191, v191, v117, v118
	v_max3_f32 v191, v191, v119, v120
	v_max3_f32 v191, v191, v121, v122
	v_max3_f32 v191, v191, v123, v124
	v_max3_f32 v191, v191, v125, v126
	v_max3_f32 v191, v191, v127, v128
	v_max_f32 v191, v191, v129
	s_nop 0
	v_max3_f32 v191, v191, v130, v131
	v_max3_f32 v191, v191, v132, v133
	v_max3_f32 v191, v191, v134, v135
	v_max3_f32 v191, v191, v136, v137
	v_max3_f32 v191, v191, v138, v139
	v_max3_f32 v191, v191, v140, v141
	v_max3_f32 v191, v191, v142, v143
	v_max3_f32 v191, v191, v144, v145
	v_mov_b32 v192, v191
	s_nop 1
	v_permlane32_swap_b32 v191, v192
	v_max_f32 v191, v191, v192
	s_nop 0
	v_cmp_ge_f32_e32 vcc, s54, v191
	s_cmp_lg_u64 vcc, exec
	s_cselect_b64 s[38:39], -1, 0
	s_cmp_eq_u64 vcc, exec
	s_cbranch_scc1 .LBB0_1270
	v_add_f32_e32 v82, 0xc0c00000, v191
	v_max_f32_e32 v82, 0, v82
	v_exp_f32_e64 v191, -v82
	v_add_f32_e32 v198, v198, v82
	v_sub_f32_e32 v114, v114, v82
	v_sub_f32_e32 v130, v130, v82
	v_sub_f32_e32 v115, v115, v82
	v_sub_f32_e32 v131, v131, v82
	v_sub_f32_e32 v116, v116, v82
	v_sub_f32_e32 v132, v132, v82
	v_sub_f32_e32 v117, v117, v82
	v_sub_f32_e32 v133, v133, v82
	v_sub_f32_e32 v118, v118, v82
	v_sub_f32_e32 v134, v134, v82
	v_sub_f32_e32 v119, v119, v82
	v_sub_f32_e32 v135, v135, v82
	v_sub_f32_e32 v120, v120, v82
	v_sub_f32_e32 v136, v136, v82
	v_sub_f32_e32 v121, v121, v82
	v_sub_f32_e32 v137, v137, v82
	v_sub_f32_e32 v122, v122, v82
	v_sub_f32_e32 v138, v138, v82
	v_sub_f32_e32 v123, v123, v82
	v_sub_f32_e32 v139, v139, v82
	v_sub_f32_e32 v124, v124, v82
	v_sub_f32_e32 v140, v140, v82
	v_sub_f32_e32 v125, v125, v82
	v_sub_f32_e32 v141, v141, v82
	v_sub_f32_e32 v126, v126, v82
	v_sub_f32_e32 v142, v142, v82
	v_sub_f32_e32 v127, v127, v82
	v_sub_f32_e32 v143, v143, v82
	v_sub_f32_e32 v128, v128, v82
	v_sub_f32_e32 v144, v144, v82
	v_sub_f32_e32 v129, v129, v82
	v_sub_f32_e32 v145, v145, v82
	v_xor_b32_e32 v82, 0x80000000, v198
	v_mov_b32_e32 v83, v82
	v_mov_b32_e32 v84, v82
	v_mov_b32_e32 v85, v82
	v_mov_b32_e32 v86, v82
	v_mov_b32_e32 v87, v82
	v_mov_b32_e32 v88, v82
	v_mov_b32_e32 v89, v82
	v_mov_b32_e32 v90, v82
	v_mov_b32_e32 v91, v82
	v_mov_b32_e32 v92, v82
	v_mov_b32_e32 v93, v82
	v_mov_b32_e32 v94, v82
	v_mov_b32_e32 v95, v82
	v_mov_b32_e32 v96, v82
	v_mov_b32_e32 v97, v82
	s_branch .LBB0_1271

.LBB0_1275:
	s_add_i32 s38, s88, s37
	s_cmpk_eq_i32 s44, 0xf9
	s_cselect_b32 s38, s77, s38
	s_ashr_i32 s39, s38, 31
	s_lshl_b64 s[38:39], s[38:39], 10
	s_mov_b32 m0, s45
	s_bitcmp1_b32 s32, 31
	s_cbranch_scc1 .Lkc_w0a_r0
	s_bitcmp1_b32 s32, 29
	s_cbranch_scc1 .Lkc_w04_r0
	s_waitcnt vmcnt(3) lgkmcnt(0)
	s_branch .Lkc_w0e_r0
.Lkc_w0a_r0:
	s_bitcmp1_b32 s32, 29
	s_cbranch_scc1 .Lkc_w05_r0
.Lkc_w04_r0:
	s_waitcnt vmcnt(4) lgkmcnt(0)
	s_branch .Lkc_w0e_r0
.Lkc_w05_r0:
	s_waitcnt vmcnt(5) lgkmcnt(0)
.Lkc_w0e_r0:
	s_and_b32 s32, s32, 0x5fffffff
	s_barrier
	v_lshl_add_u64 v[98:99], v[170:171], 0, s[38:39]
	s_add_i32 s51, s46, 0xa000
	global_load_lds_dwordx4 v[98:99], off
	v_lshl_add_u64 v[98:99], v[176:177], 0, s[60:61]
	s_mov_b32 m0, s51
	s_add_i32 s50, s46, 0xb000
	global_load_lds_dwordx4 v[98:99], off
	v_lshl_add_u64 v[98:99], v[176:177], 0, s[62:63]
	s_mov_b32 m0, s50
	v_cvt_pk_fp8_f32 v162, v114, v115
	global_load_lds_dwordx4 v[98:99], off
	v_cvt_pk_fp8_f32 v163, v118, v119
	ds_read_b128 v[210:213], v203 offset:0
	ds_read_b128 v[214:217], v204 offset:0
	ds_read_b128 v[218:221], v203 offset:0x800
	ds_read_b128 v[222:225], v204 offset:0x800
	v_cvt_pk_fp8_f32 v162, v116, v117 op_sel:[0,0,1]
	v_cvt_pk_fp8_f32 v163, v120, v121 op_sel:[0,0,1]
	s_waitcnt lgkmcnt(2)
	v_mfma_f32_32x32x64_f8f6f4 v[98:113], v[210:217], v[154:161], v[82:97]
	v_cvt_pk_fp8_f32 v164, v122, v123
	v_cvt_pk_fp8_f32 v165, v126, v127
	ds_read_b128 v[226:229], v201 offset:0
	ds_read_b128 v[230:233], v202 offset:0
	v_cvt_pk_fp8_f32 v164, v124, v125 op_sel:[0,0,1]
	v_cvt_pk_fp8_f32 v165, v128, v129 op_sel:[0,0,1]
	s_waitcnt lgkmcnt(2)
	v_mfma_f32_32x32x64_f8f6f4 v[114:129], v[218:225], v[154:161], v[82:97]
	v_cvt_pk_fp8_f32 v166, v130, v131
	v_cvt_pk_fp8_f32 v167, v134, v135
	v_cvt_pk_fp8_f32 v168, v138, v139
	v_cvt_pk_fp8_f32 v169, v142, v143
	v_cvt_pk_fp8_f32 v166, v132, v133 op_sel:[0,0,1]
	v_cvt_pk_fp8_f32 v167, v136, v137 op_sel:[0,0,1]
	v_cvt_pk_fp8_f32 v168, v140, v141 op_sel:[0,0,1]
	v_cvt_pk_fp8_f32 v169, v144, v145 op_sel:[0,0,1]
	s_nop 0
	ds_read_b128 v[138:141], v201 offset:0x800
	ds_read_b128 v[142:145], v202 offset:0x800
	s_nop 0
	v_mfma_f32_16x16x128_f8f6f4 v[18:21], v[162:169], v[146:153], v[18:21]
	s_waitcnt lgkmcnt(2)
	v_mfma_f32_32x32x64_f8f6f4 v[2:17], v[162:169], v[226:233], v[2:17]
	ds_read_b128 v[130:133], v201 offset:0x1000
	ds_read_b128 v[134:137], v202 offset:0x1000
	v_max3_f32 v191, v98, v99, v100
	v_max3_f32 v191, v191, v101, v102
	v_max3_f32 v191, v191, v103, v104
	v_max3_f32 v191, v191, v105, v106
	v_max3_f32 v191, v191, v107, v108
	v_max3_f32 v191, v191, v109, v110
	v_max3_f32 v191, v191, v111, v112
	v_max_f32 v191, v191, v113
	s_nop 0
	v_max3_f32 v191, v191, v114, v115
	v_max3_f32 v191, v191, v116, v117
	v_max3_f32 v191, v191, v118, v119
	v_max3_f32 v191, v191, v120, v121
	v_max3_f32 v191, v191, v122, v123
	v_max3_f32 v191, v191, v124, v125
	v_max3_f32 v191, v191, v126, v127
	v_max3_f32 v191, v191, v128, v129
	v_mov_b32 v192, v191
	s_nop 1
	v_permlane32_swap_b32 v191, v192
	v_max_f32 v191, v191, v192
	s_nop 0
	v_cmp_ge_f32_e32 vcc, s54, v191
	s_cmp_lg_u64 vcc, exec
	s_cselect_b64 s[38:39], -1, 0
	s_cmp_eq_u64 vcc, exec
	s_cbranch_scc1 .LBB0_1277
	v_add_f32_e32 v82, 0xc0c00000, v191
	v_max_f32_e32 v82, 0, v82
	v_exp_f32_e64 v191, -v82
	v_add_f32_e32 v198, v198, v82
	v_sub_f32_e32 v98, v98, v82
	v_sub_f32_e32 v114, v114, v82
	v_sub_f32_e32 v99, v99, v82
	v_sub_f32_e32 v115, v115, v82
	v_sub_f32_e32 v100, v100, v82
	v_sub_f32_e32 v116, v116, v82
	v_sub_f32_e32 v101, v101, v82
	v_sub_f32_e32 v117, v117, v82
	v_sub_f32_e32 v102, v102, v82
	v_sub_f32_e32 v118, v118, v82
	v_sub_f32_e32 v103, v103, v82
	v_sub_f32_e32 v119, v119, v82
	v_sub_f32_e32 v104, v104, v82
	v_sub_f32_e32 v120, v120, v82
	v_sub_f32_e32 v105, v105, v82
	v_sub_f32_e32 v121, v121, v82
	v_sub_f32_e32 v106, v106, v82
	v_sub_f32_e32 v122, v122, v82
	v_sub_f32_e32 v107, v107, v82
	v_sub_f32_e32 v123, v123, v82
	v_sub_f32_e32 v108, v108, v82
	v_sub_f32_e32 v124, v124, v82
	v_sub_f32_e32 v109, v109, v82
	v_sub_f32_e32 v125, v125, v82
	v_sub_f32_e32 v110, v110, v82
	v_sub_f32_e32 v126, v126, v82
	v_sub_f32_e32 v111, v111, v82
	v_sub_f32_e32 v127, v127, v82
	v_sub_f32_e32 v112, v112, v82
	v_sub_f32_e32 v128, v128, v82
	v_sub_f32_e32 v113, v113, v82
	v_sub_f32_e32 v129, v129, v82
	v_xor_b32_e32 v82, 0x80000000, v198
	v_mov_b32_e32 v83, v82
	v_mov_b32_e32 v84, v82
	v_mov_b32_e32 v85, v82
	v_mov_b32_e32 v86, v82
	v_mov_b32_e32 v87, v82
	v_mov_b32_e32 v88, v82
	v_mov_b32_e32 v89, v82
	v_mov_b32_e32 v90, v82
	v_mov_b32_e32 v91, v82
	v_mov_b32_e32 v92, v82
	v_mov_b32_e32 v93, v82
	v_mov_b32_e32 v94, v82
	v_mov_b32_e32 v95, v82
	v_mov_b32_e32 v96, v82
	v_mov_b32_e32 v97, v82
	s_branch .LBB0_1278

.LBB0_1282:
	s_add_i32 s44, s44, 4
	s_cmpk_lt_u32 s44, 0xfc
	s_cselect_b32 s38, s40, s41
	s_add_i32 s38, s38, s37
	s_addk_i32 s38, 0xff40
	s_ashr_i32 s39, s38, 31
	s_lshl_b64 s[38:39], s[38:39], 10
	s_waitcnt vmcnt(3) lgkmcnt(0)
	s_barrier
	v_lshl_add_u64 v[130:131], v[170:171], 0, s[38:39]
	s_add_i32 m0, s45, 0x1000
	v_cvt_pk_fp8_f32 v162, v98, v99
	global_load_lds_dwordx4 v[130:131], off
	v_lshl_add_u64 v[130:131], v[176:177], 0, s[64:65]
	s_add_i32 m0, s46, 0x4000
	v_cvt_pk_fp8_f32 v163, v102, v103
	global_load_lds_dwordx4 v[130:131], off
	v_lshl_add_u64 v[130:131], v[176:177], 0, s[66:67]
	s_add_i32 m0, s46, 0x5000
	v_cvt_pk_fp8_f32 v162, v100, v101 op_sel:[0,0,1]
	global_load_lds_dwordx4 v[130:131], off
	s_bitcmp1_b32 s32, 30
	s_cbranch_scc0 .Lkc_c9_r0
	v_mul_f32_e32 v234, 0x42000000, v234
	v_mul_f32_e32 v235, 0x42000000, v235
	v_mul_f32_e32 v236, 0x42000000, v236
	v_mul_f32_e32 v237, 0x42000000, v237
	s_nop 1
	v_permlane32_swap_b32_e32 v234, v236
	v_permlane32_swap_b32_e32 v235, v237
	s_nop 1
	v_permlane16_swap_b32_e32 v234, v235
	v_permlane16_swap_b32_e32 v236, v237
	s_nop 1
	v_cvt_pk_fp8_f32 v243, v234, v235
	v_cvt_pk_fp8_f32 v243, v236, v237 op_sel:[0,0,1]
.Lkc_c9_r0:
	ds_read_b128 v[130:133], v199 offset:0
	ds_read_b128 v[134:137], v200 offset:0
	ds_read_b128 v[210:213], v199 offset:0x800
	ds_read_b128 v[214:217], v200 offset:0x800
	v_cvt_pk_fp8_f32 v163, v104, v105 op_sel:[0,0,1]
	s_waitcnt lgkmcnt(2)
	v_cvt_pk_fp8_f32 v164, v106, v107
	v_cvt_pk_fp8_f32 v165, v110, v111
	ds_read_b128 v[218:221], v196 offset:0
	ds_read_b128 v[222:225], v197 offset:0
	v_cvt_pk_fp8_f32 v164, v108, v109 op_sel:[0,0,1]
	v_cvt_pk_fp8_f32 v165, v112, v113 op_sel:[0,0,1]
	v_mfma_f32_32x32x64_f8f6f4 v[98:113], v[130:137], v[154:161], v[82:97]
	s_waitcnt lgkmcnt(2)
	v_mfma_f32_32x32x64_f8f6f4 v[130:145], v[210:217], v[154:161], v[82:97]
	v_cvt_pk_fp8_f32 v166, v114, v115
	v_cvt_pk_fp8_f32 v167, v118, v119
	v_cvt_pk_fp8_f32 v168, v122, v123
	v_cvt_pk_fp8_f32 v169, v126, v127
	v_cvt_pk_fp8_f32 v166, v116, v117 op_sel:[0,0,1]
	v_cvt_pk_fp8_f32 v167, v120, v121 op_sel:[0,0,1]
	v_cvt_pk_fp8_f32 v168, v124, v125 op_sel:[0,0,1]
	v_cvt_pk_fp8_f32 v169, v128, v129 op_sel:[0,0,1]
	s_nop 0
	ds_read_b128 v[122:125], v196 offset:0x800
	ds_read_b128 v[126:129], v197 offset:0x800
	s_nop 0
	v_mfma_f32_16x16x128_f8f6f4 v[18:21], v[162:169], v[146:153], v[18:21]
	s_waitcnt lgkmcnt(2)
	v_mfma_f32_32x32x64_f8f6f4 v[2:17], v[162:169], v[218:225], v[2:17]
	ds_read_b128 v[114:117], v196 offset:0x1000
	ds_read_b128 v[118:121], v197 offset:0x1000
	v_max3_f32 v191, v98, v99, v100
	v_max3_f32 v191, v191, v101, v102
	v_max3_f32 v191, v191, v103, v104
	v_max3_f32 v191, v191, v105, v106
	v_max3_f32 v191, v191, v107, v108
	v_max3_f32 v191, v191, v109, v110
	v_max3_f32 v191, v191, v111, v112
	v_max_f32 v191, v191, v113
	s_nop 0
	v_max3_f32 v191, v191, v130, v131
	v_max3_f32 v191, v191, v132, v133
	v_max3_f32 v191, v191, v134, v135
	v_max3_f32 v191, v191, v136, v137
	v_max3_f32 v191, v191, v138, v139
	v_max3_f32 v191, v191, v140, v141
	v_max3_f32 v191, v191, v142, v143
	v_max3_f32 v191, v191, v144, v145
	v_mov_b32 v192, v191
	s_nop 1
	v_permlane32_swap_b32 v191, v192
	v_max_f32 v191, v191, v192
	s_nop 0
	v_cmp_ge_f32_e32 vcc, s54, v191
	s_cmp_lg_u64 vcc, exec
	s_cselect_b64 s[38:39], -1, 0
	s_cmp_eq_u64 vcc, exec
	s_cbranch_scc1 .LBB0_1284
	v_add_f32_e32 v82, 0xc0c00000, v191
	v_max_f32_e32 v82, 0, v82
	v_exp_f32_e64 v191, -v82
	v_add_f32_e32 v198, v198, v82
	v_sub_f32_e32 v98, v98, v82
	v_sub_f32_e32 v130, v130, v82
	v_sub_f32_e32 v99, v99, v82
	v_sub_f32_e32 v131, v131, v82
	v_sub_f32_e32 v100, v100, v82
	v_sub_f32_e32 v132, v132, v82
	v_sub_f32_e32 v101, v101, v82
	v_sub_f32_e32 v133, v133, v82
	v_sub_f32_e32 v102, v102, v82
	v_sub_f32_e32 v134, v134, v82
	v_sub_f32_e32 v103, v103, v82
	v_sub_f32_e32 v135, v135, v82
	v_sub_f32_e32 v104, v104, v82
	v_sub_f32_e32 v136, v136, v82
	v_sub_f32_e32 v105, v105, v82
	v_sub_f32_e32 v137, v137, v82
	v_sub_f32_e32 v106, v106, v82
	v_sub_f32_e32 v138, v138, v82
	v_sub_f32_e32 v107, v107, v82
	v_sub_f32_e32 v139, v139, v82
	v_sub_f32_e32 v108, v108, v82
	v_sub_f32_e32 v140, v140, v82
	v_sub_f32_e32 v109, v109, v82
	v_sub_f32_e32 v141, v141, v82
	v_sub_f32_e32 v110, v110, v82
	v_sub_f32_e32 v142, v142, v82
	v_sub_f32_e32 v111, v111, v82
	v_sub_f32_e32 v143, v143, v82
	v_sub_f32_e32 v112, v112, v82
	v_sub_f32_e32 v144, v144, v82
	v_sub_f32_e32 v113, v113, v82
	v_sub_f32_e32 v145, v145, v82
	v_xor_b32_e32 v82, 0x80000000, v198
	v_mov_b32_e32 v83, v82
	v_mov_b32_e32 v84, v82
	v_mov_b32_e32 v85, v82
	v_mov_b32_e32 v86, v82
	v_mov_b32_e32 v87, v82
	v_mov_b32_e32 v88, v82
	v_mov_b32_e32 v89, v82
	v_mov_b32_e32 v90, v82
	v_mov_b32_e32 v91, v82
	v_mov_b32_e32 v92, v82
	v_mov_b32_e32 v93, v82
	v_mov_b32_e32 v94, v82
	v_mov_b32_e32 v95, v82
	v_mov_b32_e32 v96, v82
	v_mov_b32_e32 v97, v82
	s_branch .LBB0_1285

.LBB0_1289:
	s_cmpk_lt_u32 s44, 0xfb
	s_cselect_b32 s38, s42, s43
	s_add_i32 s38, s38, s37
	s_addk_i32 s38, 0xff40
	s_ashr_i32 s39, s38, 31
	s_lshl_b64 s[38:39], s[38:39], 10
	s_waitcnt vmcnt(3) lgkmcnt(0)
	s_barrier
	v_lshl_add_u64 v[114:115], v[170:171], 0, s[38:39]
	s_add_i32 m0, s45, 0x2000
	v_cvt_pk_fp8_f32 v162, v98, v99
	global_load_lds_dwordx4 v[114:115], off
	v_lshl_add_u64 v[114:115], v[176:177], 0, s[68:69]
	s_add_i32 m0, s46, 0x6000
	v_cvt_pk_fp8_f32 v163, v102, v103
	global_load_lds_dwordx4 v[114:115], off
	v_lshl_add_u64 v[114:115], v[176:177], 0, s[70:71]
	s_add_i32 m0, s46, 0x7000
	v_cvt_pk_fp8_f32 v162, v100, v101 op_sel:[0,0,1]
	global_load_lds_dwordx4 v[114:115], off
	s_bitcmp1_b32 s32, 30
	s_cbranch_scc0 .Lkc_s9_r0
	s_and_b32 s100, s32, 0x3ff
	s_cmpk_lt_u32 s100, 0x100
	s_cbranch_scc0 .Lkc_sd_r0
	s_lshr_b32 s101, s100, 3
	s_lshl_b32 s101, s101, 21
	s_and_b32 s100, s100, 7
	s_lshl_b32 s100, s100, 7
	s_add_i32 s100, s100, s101
	v_readlane_b32 s101, v254, 7
	s_add_i32 s100, s100, s101
	s_branch .Lkc_sj_r0
.Lkc_sd_r0:
	s_sub_i32 s100, s100, 0x100
	s_lshr_b32 s101, s100, 2
	s_lshl_b32 s101, s101, 20
	s_and_b32 s100, s100, 3
	s_lshl_b32 s100, s100, 8
	s_add_i32 s100, s100, s101
	v_readlane_b32 s101, v254, 9
	s_add_i32 s100, s100, s101
.Lkc_sj_r0:
	v_add_u32_e32 v238, s100, v253
	v_readlane_b32 s100, v254, 4
	v_readlane_b32 s101, v254, 5
	v_mov_b32_e32 v239, 0
	s_nop 1
	v_lshl_add_u64 v[238:239], v[238:239], 0, s[100:101]
	global_store_dword v[238:239], v243, off
	s_add_i32 s32, s32, 1
	s_and_b32 s32, s32, 0xbfffffff
	s_or_b32 s32, s32, 0xa0000000
.Lkc_s9_r0:
	ds_read_b128 v[210:213], v183 offset:0
	ds_read_b128 v[214:217], v190 offset:0
	ds_read_b128 v[218:221], v183 offset:0x800
	ds_read_b128 v[222:225], v190 offset:0x800
	v_cvt_pk_fp8_f32 v163, v104, v105 op_sel:[0,0,1]
	s_waitcnt lgkmcnt(2)
	v_mfma_f32_32x32x64_f8f6f4 v[114:129], v[210:217], v[154:161], v[82:97]
	v_cvt_pk_fp8_f32 v164, v106, v107
	v_cvt_pk_fp8_f32 v165, v110, v111
	ds_read_b128 v[226:229], v194 offset:0
	ds_read_b128 v[230:233], v195 offset:0
	v_cvt_pk_fp8_f32 v164, v108, v109 op_sel:[0,0,1]
	v_cvt_pk_fp8_f32 v165, v112, v113 op_sel:[0,0,1]
	s_waitcnt lgkmcnt(2)
	v_mfma_f32_32x32x64_f8f6f4 v[98:113], v[218:225], v[154:161], v[82:97]
	v_cvt_pk_fp8_f32 v166, v130, v131
	v_cvt_pk_fp8_f32 v167, v134, v135
	v_cvt_pk_fp8_f32 v168, v138, v139
	v_cvt_pk_fp8_f32 v169, v142, v143
	v_cvt_pk_fp8_f32 v166, v132, v133 op_sel:[0,0,1]
	v_cvt_pk_fp8_f32 v167, v136, v137 op_sel:[0,0,1]
	v_cvt_pk_fp8_f32 v168, v140, v141 op_sel:[0,0,1]
	v_cvt_pk_fp8_f32 v169, v144, v145 op_sel:[0,0,1]
	s_nop 0
	ds_read_b128 v[138:141], v194 offset:0x800
	ds_read_b128 v[142:145], v195 offset:0x800
	s_nop 0
	v_mfma_f32_16x16x128_f8f6f4 v[18:21], v[162:169], v[146:153], v[18:21]
	s_waitcnt lgkmcnt(2)
	v_mfma_f32_32x32x64_f8f6f4 v[2:17], v[162:169], v[226:233], v[2:17]
	ds_read_b128 v[130:133], v194 offset:0x1000
	ds_read_b128 v[134:137], v195 offset:0x1000
	v_max3_f32 v176, v114, v115, v116
	v_max3_f32 v176, v176, v117, v118
	v_max3_f32 v176, v176, v119, v120
	v_max3_f32 v176, v176, v121, v122
	v_max3_f32 v176, v176, v123, v124
	v_max3_f32 v176, v176, v125, v126
	v_max3_f32 v176, v176, v127, v128
	v_max_f32 v176, v176, v129
	s_nop 0
	v_max3_f32 v176, v176, v98, v99
	v_max3_f32 v176, v176, v100, v101
	v_max3_f32 v176, v176, v102, v103
	v_max3_f32 v176, v176, v104, v105
	v_max3_f32 v176, v176, v106, v107
	v_max3_f32 v176, v176, v108, v109
	v_max3_f32 v176, v176, v110, v111
	v_max3_f32 v176, v176, v112, v113
	v_mov_b32 v177, v176
	s_nop 1
	v_permlane32_swap_b32 v176, v177
	v_max_f32 v176, v176, v177
	s_nop 0
	v_cmp_ge_f32_e32 vcc, s54, v176
	s_cmp_lg_u64 vcc, exec
	s_cselect_b64 s[38:39], -1, 0
	s_cmp_eq_u64 vcc, exec
	s_cbranch_scc1 .LBB0_1291
	v_add_f32_e32 v82, 0xc0c00000, v176
	v_max_f32_e32 v82, 0, v82
	v_exp_f32_e64 v176, -v82
	v_add_f32_e32 v198, v198, v82
	v_sub_f32_e32 v114, v114, v82
	v_sub_f32_e32 v98, v98, v82
	v_sub_f32_e32 v115, v115, v82
	v_sub_f32_e32 v99, v99, v82
	v_sub_f32_e32 v116, v116, v82
	v_sub_f32_e32 v100, v100, v82
	v_sub_f32_e32 v117, v117, v82
	v_sub_f32_e32 v101, v101, v82
	v_sub_f32_e32 v118, v118, v82
	v_sub_f32_e32 v102, v102, v82
	v_sub_f32_e32 v119, v119, v82
	v_sub_f32_e32 v103, v103, v82
	v_sub_f32_e32 v120, v120, v82
	v_sub_f32_e32 v104, v104, v82
	v_sub_f32_e32 v121, v121, v82
	v_sub_f32_e32 v105, v105, v82
	v_sub_f32_e32 v122, v122, v82
	v_sub_f32_e32 v106, v106, v82
	v_sub_f32_e32 v123, v123, v82
	v_sub_f32_e32 v107, v107, v82
	v_sub_f32_e32 v124, v124, v82
	v_sub_f32_e32 v108, v108, v82
	v_sub_f32_e32 v125, v125, v82
	v_sub_f32_e32 v109, v109, v82
	v_sub_f32_e32 v126, v126, v82
	v_sub_f32_e32 v110, v110, v82
	v_sub_f32_e32 v127, v127, v82
	v_sub_f32_e32 v111, v111, v82
	v_sub_f32_e32 v128, v128, v82
	v_sub_f32_e32 v112, v112, v82
	v_sub_f32_e32 v129, v129, v82
	v_sub_f32_e32 v113, v113, v82
	v_xor_b32_e32 v82, 0x80000000, v198
	v_mov_b32_e32 v83, v82
	v_mov_b32_e32 v84, v82
	v_mov_b32_e32 v85, v82
	v_mov_b32_e32 v86, v82
	v_mov_b32_e32 v87, v82
	v_mov_b32_e32 v88, v82
	v_mov_b32_e32 v89, v82
	v_mov_b32_e32 v90, v82
	v_mov_b32_e32 v91, v82
	v_mov_b32_e32 v92, v82
	v_mov_b32_e32 v93, v82
	v_mov_b32_e32 v94, v82
	v_mov_b32_e32 v95, v82
	v_mov_b32_e32 v96, v82
	v_mov_b32_e32 v97, v82
	s_branch .LBB0_1292

.Lfkc_i9_r0:
	v_cvt_pk_fp8_f32 v163, v118, v119
	ds_read_b128 v[130:133], v205 offset:0
	ds_read_b128 v[134:137], v206 offset:0
	ds_read_b128 v[210:213], v205 offset:0x800
	ds_read_b128 v[214:217], v206 offset:0x800
	v_cvt_pk_fp8_f32 v162, v116, v117 op_sel:[0,0,1]
	v_cvt_pk_fp8_f32 v163, v120, v121 op_sel:[0,0,1]
	s_waitcnt lgkmcnt(2)
	v_cvt_pk_fp8_f32 v164, v122, v123
	v_cvt_pk_fp8_f32 v165, v126, v127
	ds_read_b128 v[218:221], v188 offset:0
	ds_read_b128 v[222:225], v189 offset:0
	v_cvt_pk_fp8_f32 v164, v124, v125 op_sel:[0,0,1]
	v_cvt_pk_fp8_f32 v165, v128, v129 op_sel:[0,0,1]
	v_mfma_f32_32x32x64_f8f6f4 v[114:129], v[130:137], v[154:161], v[82:97]
	s_waitcnt lgkmcnt(2)
	v_mfma_f32_32x32x64_f8f6f4 v[130:145], v[210:217], v[154:161], v[82:97]
	v_cvt_pk_fp8_f32 v166, v98, v99
	v_cvt_pk_fp8_f32 v167, v102, v103
	v_cvt_pk_fp8_f32 v168, v106, v107
	v_cvt_pk_fp8_f32 v169, v110, v111
	v_cvt_pk_fp8_f32 v166, v100, v101 op_sel:[0,0,1]
	v_cvt_pk_fp8_f32 v167, v104, v105 op_sel:[0,0,1]
	v_cvt_pk_fp8_f32 v168, v108, v109 op_sel:[0,0,1]
	v_cvt_pk_fp8_f32 v169, v112, v113 op_sel:[0,0,1]
	s_nop 0
	ds_read_b128 v[106:109], v188 offset:0x800
	ds_read_b128 v[110:113], v189 offset:0x800
	s_nop 0
	v_mfma_f32_16x16x128_f8f6f4 v[18:21], v[162:169], v[146:153], v[18:21]
	s_waitcnt lgkmcnt(2)
	v_mfma_f32_32x32x64_f8f6f4 v[2:17], v[162:169], v[218:225], v[2:17]
	ds_read_b128 v[98:101], v188 offset:0x1000
	ds_read_b128 v[102:105], v189 offset:0x1000

.Lfkc_w0e_r0:
	s_and_b32 s32, s32, 0x5fffffff
	s_barrier
	v_lshl_add_u64 v[98:99], v[170:171], 0, s[38:39]
	s_add_i32 s51, s46, 0xa000
	global_load_lds_dwordx4 v[98:99], off
	v_lshl_add_u64 v[98:99], v[176:177], 0, s[60:61]
	s_mov_b32 m0, s51
	s_add_i32 s50, s46, 0xb000
	global_load_lds_dwordx4 v[98:99], off
	v_lshl_add_u64 v[98:99], v[176:177], 0, s[62:63]
	s_mov_b32 m0, s50
	v_cvt_pk_fp8_f32 v162, v114, v115
	global_load_lds_dwordx4 v[98:99], off
	v_cvt_pk_fp8_f32 v163, v118, v119
	ds_read_b128 v[210:213], v203 offset:0
	ds_read_b128 v[214:217], v204 offset:0
	ds_read_b128 v[218:221], v203 offset:0x800
	ds_read_b128 v[222:225], v204 offset:0x800
	v_cvt_pk_fp8_f32 v162, v116, v117 op_sel:[0,0,1]
	v_cvt_pk_fp8_f32 v163, v120, v121 op_sel:[0,0,1]
	s_waitcnt lgkmcnt(2)
	v_mfma_f32_32x32x64_f8f6f4 v[98:113], v[210:217], v[154:161], v[82:97]
	v_cvt_pk_fp8_f32 v164, v122, v123
	v_cvt_pk_fp8_f32 v165, v126, v127
	ds_read_b128 v[226:229], v201 offset:0
	ds_read_b128 v[230:233], v202 offset:0
	v_cvt_pk_fp8_f32 v164, v124, v125 op_sel:[0,0,1]
	v_cvt_pk_fp8_f32 v165, v128, v129 op_sel:[0,0,1]
	s_waitcnt lgkmcnt(2)
	v_mfma_f32_32x32x64_f8f6f4 v[114:129], v[218:225], v[154:161], v[82:97]
	v_cvt_pk_fp8_f32 v166, v130, v131
	v_cvt_pk_fp8_f32 v167, v134, v135
	v_cvt_pk_fp8_f32 v168, v138, v139
	v_cvt_pk_fp8_f32 v169, v142, v143
	v_cvt_pk_fp8_f32 v166, v132, v133 op_sel:[0,0,1]
	v_cvt_pk_fp8_f32 v167, v136, v137 op_sel:[0,0,1]
	v_cvt_pk_fp8_f32 v168, v140, v141 op_sel:[0,0,1]
	v_cvt_pk_fp8_f32 v169, v144, v145 op_sel:[0,0,1]
	s_nop 0
	ds_read_b128 v[138:141], v201 offset:0x800
	ds_read_b128 v[142:145], v202 offset:0x800
	s_nop 0
	v_mfma_f32_16x16x128_f8f6f4 v[18:21], v[162:169], v[146:153], v[18:21]
	s_waitcnt lgkmcnt(2)
	v_mfma_f32_32x32x64_f8f6f4 v[2:17], v[162:169], v[226:233], v[2:17]
	ds_read_b128 v[130:133], v201 offset:0x1000
	ds_read_b128 v[134:137], v202 offset:0x1000

.Lfkc_c9_r0:
	ds_read_b128 v[130:133], v199 offset:0
	ds_read_b128 v[134:137], v200 offset:0
	ds_read_b128 v[210:213], v199 offset:0x800
	ds_read_b128 v[214:217], v200 offset:0x800
	v_cvt_pk_fp8_f32 v163, v104, v105 op_sel:[0,0,1]
	s_waitcnt lgkmcnt(2)
	v_cvt_pk_fp8_f32 v164, v106, v107
	v_cvt_pk_fp8_f32 v165, v110, v111
	ds_read_b128 v[218:221], v196 offset:0
	ds_read_b128 v[222:225], v197 offset:0
	v_cvt_pk_fp8_f32 v164, v108, v109 op_sel:[0,0,1]
	v_cvt_pk_fp8_f32 v165, v112, v113 op_sel:[0,0,1]
	v_mfma_f32_32x32x64_f8f6f4 v[98:113], v[130:137], v[154:161], v[82:97]
	s_waitcnt lgkmcnt(2)
	v_mfma_f32_32x32x64_f8f6f4 v[130:145], v[210:217], v[154:161], v[82:97]
	v_cvt_pk_fp8_f32 v166, v114, v115
	v_cvt_pk_fp8_f32 v167, v118, v119
	v_cvt_pk_fp8_f32 v168, v122, v123
	v_cvt_pk_fp8_f32 v169, v126, v127
	v_cvt_pk_fp8_f32 v166, v116, v117 op_sel:[0,0,1]
	v_cvt_pk_fp8_f32 v167, v120, v121 op_sel:[0,0,1]
	v_cvt_pk_fp8_f32 v168, v124, v125 op_sel:[0,0,1]
	v_cvt_pk_fp8_f32 v169, v128, v129 op_sel:[0,0,1]
	s_nop 0
	ds_read_b128 v[122:125], v196 offset:0x800
	ds_read_b128 v[126:129], v197 offset:0x800
	s_nop 0
	v_mfma_f32_16x16x128_f8f6f4 v[18:21], v[162:169], v[146:153], v[18:21]
	s_waitcnt lgkmcnt(2)
	v_mfma_f32_32x32x64_f8f6f4 v[2:17], v[162:169], v[218:225], v[2:17]
	ds_read_b128 v[114:117], v196 offset:0x1000
	ds_read_b128 v[118:121], v197 offset:0x1000

.Lfkc_s9_r0:
	ds_read_b128 v[210:213], v183 offset:0
	ds_read_b128 v[214:217], v190 offset:0
	ds_read_b128 v[218:221], v183 offset:0x800
	ds_read_b128 v[222:225], v190 offset:0x800
	v_cvt_pk_fp8_f32 v163, v104, v105 op_sel:[0,0,1]
	s_waitcnt lgkmcnt(2)
	v_mfma_f32_32x32x64_f8f6f4 v[114:129], v[210:217], v[154:161], v[82:97]
	v_cvt_pk_fp8_f32 v164, v106, v107
	v_cvt_pk_fp8_f32 v165, v110, v111
	ds_read_b128 v[226:229], v194 offset:0
	ds_read_b128 v[230:233], v195 offset:0
	v_cvt_pk_fp8_f32 v164, v108, v109 op_sel:[0,0,1]
	v_cvt_pk_fp8_f32 v165, v112, v113 op_sel:[0,0,1]
	s_waitcnt lgkmcnt(2)
	v_mfma_f32_32x32x64_f8f6f4 v[98:113], v[218:225], v[154:161], v[82:97]
	v_cvt_pk_fp8_f32 v166, v130, v131
	v_cvt_pk_fp8_f32 v167, v134, v135
	v_cvt_pk_fp8_f32 v168, v138, v139
	v_cvt_pk_fp8_f32 v169, v142, v143
	v_cvt_pk_fp8_f32 v166, v132, v133 op_sel:[0,0,1]
	v_cvt_pk_fp8_f32 v167, v136, v137 op_sel:[0,0,1]
	v_cvt_pk_fp8_f32 v168, v140, v141 op_sel:[0,0,1]
	v_cvt_pk_fp8_f32 v169, v144, v145 op_sel:[0,0,1]
	s_nop 0
	ds_read_b128 v[138:141], v194 offset:0x800
	ds_read_b128 v[142:145], v195 offset:0x800
	s_nop 0
	v_mfma_f32_16x16x128_f8f6f4 v[18:21], v[162:169], v[146:153], v[18:21]
	s_waitcnt lgkmcnt(2)
	v_mfma_f32_32x32x64_f8f6f4 v[2:17], v[162:169], v[226:233], v[2:17]
	ds_read_b128 v[130:133], v194 offset:0x1000
	ds_read_b128 v[134:137], v195 offset:0x1000

.LBB0_1376:
	s_and_b64 vcc, exec, s[38:39]
	s_cbranch_vccz .LBB0_1202
	ds_read_b128 v[18:21], v183 offset:0
	ds_read_b128 v[22:25], v190 offset:0
	ds_read_b128 v[34:37], v183 offset:0x800
	ds_read_b128 v[38:41], v190 offset:0x800
	s_waitcnt lgkmcnt(0)
	s_waitcnt vmcnt(0)
	s_nop 11
	v_mfma_f32_32x32x64_f8f6f4 v[18:33], v[18:25], v[154:161], 0
	s_mov_b32 s37, s36
	s_mov_b32 s38, s36
	s_mov_b32 s39, s36
	s_mov_b32 s40, s36
	s_mov_b32 s41, s36
	s_mov_b32 s42, s36
	s_mov_b32 s43, s36
	s_mov_b32 s44, s36
	s_mov_b32 s45, s36
	s_mov_b32 s46, s36
	s_mov_b32 s47, s36
	s_mov_b32 s48, s36
	s_mov_b32 s49, s36
	s_mov_b32 s50, s36
	s_mov_b32 s51, s36
	v_mov_b64_e32 v[2:3], s[36:37]
	v_mov_b64_e32 v[4:5], s[38:39]
	v_mov_b64_e32 v[6:7], s[40:41]
	v_mov_b64_e32 v[8:9], s[42:43]
	v_mov_b64_e32 v[10:11], s[44:45]
	v_mov_b64_e32 v[12:13], s[46:47]
	v_mov_b64_e32 v[14:15], s[48:49]
	v_mov_b64_e32 v[16:17], s[50:51]
	v_max_f32_e32 v42, v19, v19
	v_max_f32_e32 v43, v18, v18
	v_max_f32_e32 v42, v43, v42
	v_max3_f32 v42, v42, v20, v21
	v_max3_f32 v42, v42, v22, v23
	v_max3_f32 v42, v42, v24, v25
	v_max3_f32 v42, v42, v26, v27
	v_max3_f32 v42, v42, v28, v29
	v_max3_f32 v50, v42, v30, v31
	v_mfma_f32_32x32x64_f8f6f4 v[34:49], v[34:41], v[154:161], 0
	v_max3_f32 v50, v50, v32, v33
	s_lshl_b32 s45, s95, 10
	s_lshl_b32 s46, s81, 10
	s_cmp_lg_u32 0, -1
	s_cselect_b32 s38, 0, 0
	s_add_i32 s37, s38, 0x2000
	s_add_i32 s39, s38, 0x3000
	s_add_i32 s6, s38, 0x1000
	v_add_u32_e32 v203, s37, v194
	s_add_i32 s37, s38, 0x6000
	v_add_u32_e32 v199, s39, v194
	s_add_i32 s39, s38, 0x8000
	s_add_i32 s38, s38, 0xa000
	v_add_u32_e32 v205, s6, v194
	v_add_u32_e32 v201, s37, v194
	s_nop 4
	v_max3_f32 v50, v50, v34, v35
	v_max3_f32 v50, v50, v36, v37
	v_max3_f32 v50, v50, v38, v39
	v_max3_f32 v50, v50, v40, v41
	v_max3_f32 v50, v50, v42, v43
	v_max3_f32 v50, v50, v44, v45
	v_max3_f32 v50, v50, v46, v47
	v_max3_f32 v50, v50, v48, v49
	v_mov_b32_e32 v51, v50
	s_nop 1
	v_permlane32_swap_b32_e32 v50, v51
	v_max_f32_e32 v51, v51, v51
	v_max_f32_e32 v50, v50, v50
	v_max_f32_e32 v50, v50, v51
	s_cmp_eq_u32 s98, 0
	s_cselect_b32 s100, 0x40000000, 0xc0600000
	v_add_f32_e32 v198, s100, v50
	v_sub_f32_e32 v18, v18, v198
	v_sub_f32_e32 v19, v19, v198
	v_add_u32_e32 v196, s39, v194
	v_add_u32_e32 v194, s38, v194
	s_lshl_b32 s38, s80, 4
	v_exp_f32_e32 v114, v18
	v_exp_f32_e32 v115, v19
	v_lshl_add_u64 v[18:19], s[16:17], 0, v[180:181]
	s_and_b32 s38, s38, 0xfffffc00
	s_ashr_i32 s89, s88, 31
	s_or_b32 s40, s88, 0x100
	s_add_i32 s41, s94, 0x4100
	s_or_b32 s42, s88, 0x140
	s_add_i32 s43, s94, 0x4140
	v_lshl_add_u64 v[170:171], v[18:19], 0, s[28:29]
	v_lshl_or_b32 v18, v193, 4, s38
	s_lshl_b64 s[38:39], s[88:89], 10
	s_add_u32 s38, s38, s87
	v_xor_b32_e32 v82, 0x80000000, v198
	v_sub_f32_e32 v34, v34, v198
	v_sub_f32_e32 v35, v35, v198
	v_sub_f32_e32 v20, v20, v198
	v_sub_f32_e32 v36, v36, v198
	v_sub_f32_e32 v21, v21, v198
	v_sub_f32_e32 v37, v37, v198
	v_sub_f32_e32 v22, v22, v198
	v_sub_f32_e32 v38, v38, v198
	v_sub_f32_e32 v23, v23, v198
	v_sub_f32_e32 v39, v39, v198
	v_sub_f32_e32 v24, v24, v198
	v_sub_f32_e32 v40, v40, v198
	v_sub_f32_e32 v25, v25, v198
	v_sub_f32_e32 v41, v41, v198
	v_sub_f32_e32 v26, v26, v198
	v_sub_f32_e32 v42, v42, v198
	v_sub_f32_e32 v27, v27, v198
	v_sub_f32_e32 v43, v43, v198
	v_sub_f32_e32 v28, v28, v198
	v_sub_f32_e32 v44, v44, v198
	v_sub_f32_e32 v29, v29, v198
	v_sub_f32_e32 v45, v45, v198
	v_sub_f32_e32 v30, v30, v198
	v_sub_f32_e32 v46, v46, v198
	v_sub_f32_e32 v31, v31, v198
	v_sub_f32_e32 v47, v47, v198
	v_sub_f32_e32 v32, v32, v198
	v_sub_f32_e32 v48, v48, v198
	v_sub_f32_e32 v33, v33, v198
	v_sub_f32_e32 v49, v49, v198
	s_addc_u32 s39, s39, s76
	v_mov_b32_e32 v83, v82
	v_mov_b32_e32 v84, v82
	v_mov_b32_e32 v85, v82
	v_mov_b32_e32 v86, v82
	v_mov_b32_e32 v87, v82
	v_mov_b32_e32 v88, v82
	v_mov_b32_e32 v89, v82
	v_mov_b32_e32 v90, v82
	v_mov_b32_e32 v91, v82
	v_mov_b32_e32 v92, v82
	v_mov_b32_e32 v93, v82
	v_mov_b32_e32 v94, v82
	v_mov_b32_e32 v95, v82
	v_mov_b32_e32 v96, v82
	v_mov_b32_e32 v97, v82
	v_exp_f32_e32 v98, v34
	v_exp_f32_e32 v99, v35
	v_exp_f32_e32 v116, v20
	v_exp_f32_e32 v100, v36
	v_exp_f32_e32 v117, v21
	v_exp_f32_e32 v101, v37
	v_exp_f32_e32 v118, v22
	v_exp_f32_e32 v102, v38
	v_exp_f32_e32 v119, v23
	v_exp_f32_e32 v103, v39
	v_exp_f32_e32 v120, v24
	v_exp_f32_e32 v104, v40
	v_exp_f32_e32 v121, v25
	v_exp_f32_e32 v105, v41
	v_exp_f32_e32 v122, v26
	v_exp_f32_e32 v106, v42
	v_exp_f32_e32 v123, v27
	v_exp_f32_e32 v107, v43
	v_exp_f32_e32 v124, v28
	v_exp_f32_e32 v108, v44
	v_exp_f32_e32 v125, v29
	v_exp_f32_e32 v109, v45
	v_exp_f32_e32 v126, v30
	v_exp_f32_e32 v110, v46
	v_exp_f32_e32 v127, v31
	v_exp_f32_e32 v111, v47
	v_exp_f32_e32 v128, v32
	v_exp_f32_e32 v112, v48
	v_exp_f32_e32 v129, v33
	v_exp_f32_e32 v113, v49
	v_mov_b32_e32 v19, v181
	s_add_u32 s38, s38, 0x29c30040
	s_waitcnt vmcnt(3) lgkmcnt(0)
	s_barrier
	v_lshl_add_u64 v[172:173], s[92:93], 0, v[18:19]
	s_addc_u32 s39, s39, 0
	v_add3_u32 v18, s79, v191, v192
	v_lshl_add_u64 v[174:175], s[38:39], 0, v[18:19]
	v_mov_b32_e32 v162, 0
	v_mov_b64_e32 v[48:49], v[16:17]
	v_mov_b64_e32 v[64:65], v[16:17]
	v_mov_b64_e32 v[80:81], v[16:17]
	v_mov_b64_e32 v[32:33], v[16:17]
	v_add_u32_e32 v206, v205, v195
	v_cmp_gt_u32_e64 s[6:7], 32, v193
	v_add_u32_e32 v204, v203, v195
	v_add_u32_e32 v202, v201, v195
	s_movk_i32 s37, 0x100
	v_add_u32_e32 v200, v199, v195
	v_add_u32_e32 v197, v196, v195
	v_add_u32_e32 v195, v194, v195
	s_mov_b32 s44, -3
	s_add_i32 s45, s45, 0
	s_add_i32 s46, s46, 0
	v_mov_b64_e32 v[46:47], v[14:15]
	v_mov_b64_e32 v[44:45], v[12:13]
	v_mov_b64_e32 v[42:43], v[10:11]
	v_mov_b64_e32 v[40:41], v[8:9]
	v_mov_b64_e32 v[38:39], v[6:7]
	v_mov_b64_e32 v[36:37], v[4:5]
	v_mov_b64_e32 v[34:35], v[2:3]
	v_mov_b64_e32 v[62:63], v[14:15]
	v_mov_b64_e32 v[60:61], v[12:13]
	v_mov_b64_e32 v[58:59], v[10:11]
	v_mov_b64_e32 v[56:57], v[8:9]
	v_mov_b64_e32 v[54:55], v[6:7]
	v_mov_b64_e32 v[52:53], v[4:5]
	v_mov_b64_e32 v[50:51], v[2:3]
	v_mov_b64_e32 v[78:79], v[14:15]
	v_mov_b64_e32 v[76:77], v[12:13]
	v_mov_b64_e32 v[74:75], v[10:11]
	v_mov_b64_e32 v[72:73], v[8:9]
	v_mov_b64_e32 v[70:71], v[6:7]
	v_mov_b64_e32 v[68:69], v[4:5]
	v_mov_b64_e32 v[66:67], v[2:3]
	v_mov_b64_e32 v[30:31], v[14:15]
	v_mov_b64_e32 v[28:29], v[12:13]
	v_mov_b64_e32 v[26:27], v[10:11]
	v_mov_b64_e32 v[24:25], v[8:9]
	v_mov_b64_e32 v[22:23], v[6:7]
	v_mov_b64_e32 v[20:21], v[4:5]
	v_mov_b64_e32 v[18:19], v[2:3]
	v_mov_b32_e32 v163, v162
	v_mov_b32_e32 v164, v162
	v_mov_b32_e32 v165, v162
	v_mov_b32_e32 v166, v162
	v_mov_b32_e32 v167, v162
	v_mov_b32_e32 v168, v162
	v_mov_b32_e32 v169, v162
	s_and_b32 s32, s32, 0x5fffffff
	s_cmp_lg_u32 s98, 0
	s_cbranch_scc1 .LBB0_1380
	s_branch .Lf_1380
